# speedup vs baseline: 1.0324x; 1.0123x over previous
_Z6k_prepPKiPKfPiS3_P15HIP_vector_typeIjLj4EEPh:
	s_mov_b64 s[4:5], -1
	s_cmpk_gt_i32 s2, 0xff
	v_lshl_or_b32 v2, s2, 9, v0
	s_cbranch_scc0 .LBB0_20
	v_add_u32_e32 v3, 0xfffe0000, v2
	s_movk_i32 s3, 0x1300
	v_cmp_gt_i32_e32 vcc, s3, v3
	s_and_saveexec_b64 s[4:5], vcc
	s_cbranch_execz .LBB0_19
	s_load_dwordx2 s[6:7], s[0:1], 0x8
	s_load_dwordx2 s[8:9], s[0:1], 0x20
	v_bfe_u32 v1, v0, 6, 2
	v_and_b32_e32 v4, 15, v0
	v_lshl_or_b32 v4, v1, 4, v4
	v_lshrrev_b32_e32 v5, 1, v0
	v_lshrrev_b32_e32 v3, 8, v3
	v_and_b32_e32 v5, 24, v5
	v_mul_u32_u24_e32 v4, 0x4b0, v4
	v_lshl_or_b32 v8, v3, 5, v5
	v_lshlrev_b32_e32 v4, 2, v4
	v_mov_b32_e32 v5, 0
	s_movk_i32 s3, 0x258
	v_mov_b32_e32 v9, 0
	v_mov_b32_e32 v12, 0
	v_mov_b32_e32 v13, 0
	v_mov_b32_e32 v14, 0
	v_mov_b32_e32 v15, 0
	v_mov_b32_e32 v16, 0
	v_mov_b32_e32 v17, 0
	v_mov_b32_e32 v18, 0
	v_mov_b32_e32 v19, 0
	v_mov_b32_e32 v20, 0
	v_mov_b32_e32 v21, 0
	v_mov_b32_e32 v22, 0
	v_mov_b32_e32 v23, 0
	v_mov_b32_e32 v24, 0
	v_mov_b32_e32 v25, 0
	v_mov_b32_e32 v26, 0
	v_mov_b32_e32 v27, 0
	s_waitcnt lgkmcnt(0)
	v_lshl_add_u64 v[6:7], s[6:7], 0, v[4:5]
	v_cmp_gt_u32_e32 vcc, s3, v8
	v_lshlrev_b32_e32 v8, 3, v8
	v_lshl_add_u64 v[10:11], v[6:7], 0, v[8:9]
	s_and_saveexec_b64 s[6:7], vcc
	global_load_dwordx4 v[12:15], v[10:11], off
	global_load_dwordx4 v[16:19], v[10:11], off offset:16
	global_load_dwordx4 v[20:23], v[10:11], off offset:32
	global_load_dwordx4 v[24:27], v[10:11], off offset:48
	s_or_b64 exec, exec, s[6:7]
	v_and_b32_e32 v4, 63, v0
	v_lshlrev_b32_e32 v3, 9, v3
	v_lshlrev_b32_e32 v1, 6, v1
	v_or3_b32 v4, v3, v1, v4
	v_mov_b32_e32 v5, 0
	v_lshl_add_u64 v[10:11], v[4:5], 4, s[8:9]
	v_add_u32_e32 v4, 0x100, v4
	v_lshl_add_u64 v[4:5], v[4:5], 4, s[8:9]
	s_waitcnt vmcnt(0)
	v_cvt_pk_f16_f32 v28, v12, v14
	v_cvt_pk_f16_f32 v29, v16, v18
	v_cvt_pk_f16_f32 v30, v20, v22
	v_cvt_pk_f16_f32 v31, v24, v26
	v_cvt_pk_f16_f32 v32, v13, v15
	v_cvt_pk_f16_f32 v33, v17, v19
	v_cvt_pk_f16_f32 v34, v21, v23
	v_cvt_pk_f16_f32 v35, v25, v27
	global_store_dwordx4 v[10:11], v[28:31], off
	global_store_dwordx4 v[4:5], v[32:35], off

	.amdhsa_kernel _Z6k_prepPKiPKfPiS3_P15HIP_vector_typeIjLj4EEPh
		.amdhsa_group_segment_fixed_size 32
		.amdhsa_private_segment_fixed_size 0
		.amdhsa_kernarg_size 48
		.amdhsa_user_sgpr_count 2
		.amdhsa_user_sgpr_dispatch_ptr 0
		.amdhsa_user_sgpr_queue_ptr 0
		.amdhsa_user_sgpr_kernarg_segment_ptr 1
		.amdhsa_user_sgpr_dispatch_id 0
		.amdhsa_user_sgpr_kernarg_preload_length 0
		.amdhsa_user_sgpr_kernarg_preload_offset 0
		.amdhsa_user_sgpr_private_segment_size 0
		.amdhsa_uses_dynamic_stack 0
		.amdhsa_enable_private_segment 0
		.amdhsa_system_sgpr_workgroup_id_x 1
		.amdhsa_system_sgpr_workgroup_id_y 0
		.amdhsa_system_sgpr_workgroup_id_z 0
		.amdhsa_system_sgpr_workgroup_info 0
		.amdhsa_system_vgpr_workitem_id 0
		.amdhsa_next_free_vgpr 36
		.amdhsa_next_free_sgpr 10
		.amdhsa_accum_offset 36
		.amdhsa_reserve_vcc 1
		.amdhsa_float_round_mode_32 0
		.amdhsa_float_round_mode_16_64 0
		.amdhsa_float_denorm_mode_32 3
		.amdhsa_float_denorm_mode_16_64 3
		.amdhsa_dx10_clamp 1
		.amdhsa_ieee_mode 1
		.amdhsa_fp16_overflow 0
		.amdhsa_tg_split 0
		.amdhsa_exception_fp_ieee_invalid_op 0
		.amdhsa_exception_fp_denorm_src 0
		.amdhsa_exception_fp_ieee_div_zero 0
		.amdhsa_exception_fp_ieee_overflow 0
		.amdhsa_exception_fp_ieee_underflow 0
		.amdhsa_exception_fp_ieee_inexact 0
		.amdhsa_exception_int_div_zero 0
	.end_amdhsa_kernel

_Z6k_poolPKDF16_PKiS2_PKfS4_S4_Pf:
	s_load_dwordx8 s[4:11], s[0:1], 0x0
	s_ashr_i32 s3, s2, 31
	s_lshl_b64 s[12:13], s[2:3], 2
	v_lshrrev_b32_e32 v37, 4, v0
	v_bfe_u32 v1, v0, 3, 1
	s_waitcnt lgkmcnt(0)
	s_add_u32 s6, s6, s12
	s_addc_u32 s7, s7, s13
	s_lshl_b32 s12, s2, 9
	s_ashr_i32 s13, s12, 31
	s_lshl_b64 s[12:13], s[12:13], 2
	s_add_u32 s8, s8, s12
	v_add_u32_e32 v1, v1, v37
	s_addc_u32 s9, s9, s13
	v_lshlrev_b32_e32 v3, 2, v1
	global_load_dword v2, v3, s[8:9]
	global_load_dword v4, v3, s[8:9] offset:256
	global_load_dword v10, v3, s[8:9] offset:512
	global_load_dword v14, v3, s[8:9] offset:768
	global_load_dword v18, v3, s[8:9] offset:1024
	global_load_dword v24, v3, s[8:9] offset:1280
	v_min_u32_e32 v1, 63, v1
	v_lshlrev_b32_e32 v1, 2, v1
	global_load_dword v6, v3, s[8:9] offset:1536
	global_load_dword v8, v1, s[8:9] offset:1792
	v_and_b32_e32 v36, 15, v0
	v_mov_b32_e32 v13, 0
	v_lshlrev_b32_e32 v12, 4, v36
	v_lshl_add_u64 v[22:23], s[4:5], 0, v[12:13]
	v_mbcnt_lo_u32_b32 v1, -1, 0
	s_load_dwordx2 s[4:5], s[0:1], 0x20
	v_mbcnt_hi_u32_b32 v1, -1, v1
	v_and_b32_e32 v38, 63, v0
	v_and_b32_e32 v9, 56, v1
	v_lshlrev_b32_e32 v7, 2, v38
	v_cmp_eq_u32_e32 vcc, 56, v9
	s_load_dword s6, s[6:7], 0x0
	v_mov_b32_e32 v40, 0xfc00fc00
	v_cndmask_b32_e64 v9, 8, 0, vcc
	v_add_lshl_u32 v49, v9, v1, 2
	v_or_b32_e32 v41, 64, v37
	v_or_b32_e32 v46, 0x80, v37
	s_mov_b32 s3, 0xfc00
	v_or_b32_e32 v47, 0xc0, v37
	v_or_b32_e32 v48, 0x100, v37
	s_waitcnt vmcnt(7)
	v_ashrrev_i32_e32 v3, 31, v2
	v_lshlrev_b64 v[2:3], 8, v[2:3]
	v_lshl_add_u64 v[2:3], v[22:23], 0, v[2:3]
	s_waitcnt vmcnt(6)
	v_ashrrev_i32_e32 v5, 31, v4
	global_load_dwordx4 v[30:33], v[2:3], off nt
	v_lshlrev_b64 v[2:3], 8, v[4:5]
	v_lshl_add_u64 v[2:3], v[22:23], 0, v[2:3]
	s_waitcnt vmcnt(6)
	v_ashrrev_i32_e32 v11, 31, v10
	global_load_dwordx4 v[26:29], v[2:3], off nt
	v_lshlrev_b64 v[2:3], 8, v[10:11]
	v_lshl_add_u64 v[2:3], v[22:23], 0, v[2:3]
	s_waitcnt vmcnt(6)
	v_ashrrev_i32_e32 v15, 31, v14
	global_load_dwordx4 v[10:13], v[2:3], off nt
	v_lshlrev_b64 v[2:3], 8, v[14:15]
	v_lshl_add_u64 v[2:3], v[22:23], 0, v[2:3]
	s_waitcnt vmcnt(6)
	v_ashrrev_i32_e32 v19, 31, v18
	global_load_dwordx4 v[14:17], v[2:3], off nt
	v_lshlrev_b64 v[2:3], 8, v[18:19]
	v_lshl_add_u64 v[2:3], v[22:23], 0, v[2:3]
	s_waitcnt vmcnt(6)
	v_ashrrev_i32_e32 v25, 31, v24
	global_load_dwordx4 v[18:21], v[2:3], off nt
	v_lshlrev_b64 v[2:3], 8, v[24:25]
	v_lshl_add_u64 v[2:3], v[22:23], 0, v[2:3]
	global_load_dwordx4 v[2:5], v[2:3], off nt
	s_nop 0
	global_load_dword v39, v7, s[10:11]
	s_waitcnt lgkmcnt(0)
	global_load_dword v34, v7, s[4:5]
	global_load_dword v35, v7, s[4:5] offset:256
	s_waitcnt vmcnt(10)
	v_ashrrev_i32_e32 v7, 31, v6
	s_waitcnt vmcnt(9)
	v_ashrrev_i32_e32 v9, 31, v8
	v_lshlrev_b64 v[6:7], 8, v[6:7]
	v_lshlrev_b64 v[8:9], 8, v[8:9]
	v_lshl_add_u64 v[42:43], v[22:23], 0, v[6:7]
	v_lshl_add_u64 v[44:45], v[22:23], 0, v[8:9]
	global_load_dwordx4 v[22:25], v[42:43], off nt
	global_load_dwordx4 v[6:9], v[44:45], off nt
	s_min_i32 s4, s6, 0x1ff
	v_cmp_gt_i32_e32 vcc, s4, v37
	s_waitcnt vmcnt(10)
	ds_bpermute_b32 v42, v49, v30
	ds_bpermute_b32 v43, v49, v31
	ds_bpermute_b32 v44, v49, v32
	ds_bpermute_b32 v45, v49, v33
	s_waitcnt vmcnt(9)
	ds_bpermute_b32 v50, v49, v26
	ds_bpermute_b32 v51, v49, v27
	ds_bpermute_b32 v52, v49, v28
	ds_bpermute_b32 v53, v49, v29
	s_waitcnt vmcnt(8)
	ds_bpermute_b32 v54, v49, v10
	ds_bpermute_b32 v55, v49, v11
	ds_bpermute_b32 v56, v49, v12
	ds_bpermute_b32 v57, v49, v13
	s_waitcnt vmcnt(7)
	ds_bpermute_b32 v58, v49, v14
	ds_bpermute_b32 v59, v49, v15
	s_waitcnt lgkmcnt(13)
	v_pk_add_f16 v30, v30, v42
	s_waitcnt lgkmcnt(12)
	v_pk_add_f16 v31, v31, v43
	s_waitcnt lgkmcnt(11)
	v_pk_add_f16 v32, v32, v44
	s_waitcnt lgkmcnt(10)
	v_pk_add_f16 v33, v33, v45
	ds_bpermute_b32 v42, v49, v16
	ds_bpermute_b32 v43, v49, v17
	s_waitcnt vmcnt(6)
	ds_bpermute_b32 v44, v49, v18
	ds_bpermute_b32 v45, v49, v19
	s_waitcnt lgkmcnt(13)
	v_pk_add_f16 v26, v26, v50
	s_waitcnt lgkmcnt(12)
	v_pk_add_f16 v27, v27, v51
	s_waitcnt lgkmcnt(11)
	v_pk_add_f16 v28, v28, v52
	s_waitcnt lgkmcnt(10)
	v_pk_add_f16 v29, v29, v53
	ds_bpermute_b32 v50, v49, v20
	ds_bpermute_b32 v51, v49, v21
	v_cndmask_b32_e32 v30, v40, v30, vcc
	v_cndmask_b32_e32 v31, v40, v31, vcc
	v_cndmask_b32_e32 v32, v40, v32, vcc
	v_cndmask_b32_e32 v33, v40, v33, vcc
	v_cmp_gt_i32_e32 vcc, s4, v41
	s_waitcnt vmcnt(5)
	ds_bpermute_b32 v52, v49, v2
	s_waitcnt lgkmcnt(12)
	v_pk_add_f16 v10, v10, v54
	s_waitcnt lgkmcnt(11)
	v_pk_add_f16 v11, v11, v55
	s_waitcnt lgkmcnt(10)
	v_pk_add_f16 v12, v12, v56
	s_waitcnt lgkmcnt(9)
	v_pk_add_f16 v13, v13, v57
	v_cndmask_b32_e32 v26, v40, v26, vcc
	v_cndmask_b32_e32 v27, v40, v27, vcc
	v_cndmask_b32_e32 v28, v40, v28, vcc
	v_cndmask_b32_e32 v29, v40, v29, vcc
	v_cmp_gt_i32_e32 vcc, s4, v46
	v_pk_max_f16 v30, v30, v30
	v_pk_max_f16 v31, v31, v31
	s_waitcnt lgkmcnt(8)
	v_pk_add_f16 v14, v14, v58
	s_waitcnt lgkmcnt(7)
	v_pk_add_f16 v15, v15, v59
	v_cndmask_b32_e32 v10, v40, v10, vcc
	v_cndmask_b32_e32 v11, v40, v11, vcc
	v_cndmask_b32_e32 v12, v40, v12, vcc
	v_cndmask_b32_e32 v13, v40, v13, vcc
	v_cmp_gt_i32_e32 vcc, s4, v47
	v_pk_max_f16 v26, v26, v26
	v_pk_max_f16 v27, v27, v27
	v_pk_max_f16 v30, v30, s3 op_sel_hi:[1,0]
	v_pk_max_f16 v31, v31, s3 op_sel_hi:[1,0]
	v_cndmask_b32_e32 v14, v40, v14, vcc
	v_cndmask_b32_e32 v15, v40, v15, vcc
	v_pk_max_f16 v10, v10, v10
	v_pk_max_f16 v11, v11, v11
	v_pk_max_f16 v26, v30, v26
	v_pk_max_f16 v27, v31, v27
	s_waitcnt lgkmcnt(6)
	v_pk_add_f16 v16, v16, v42
	s_waitcnt lgkmcnt(5)
	v_pk_add_f16 v17, v17, v43
	v_pk_max_f16 v14, v14, v14
	v_pk_max_f16 v15, v15, v15
	v_pk_max_f16 v10, v26, v10
	v_pk_max_f16 v11, v27, v11
	s_waitcnt lgkmcnt(4)
	v_pk_add_f16 v18, v18, v44
	s_waitcnt lgkmcnt(3)
	v_pk_add_f16 v19, v19, v45
	s_waitcnt lgkmcnt(2)
	v_pk_add_f16 v20, v20, v50
	s_waitcnt lgkmcnt(1)
	v_pk_add_f16 v21, v21, v51
	v_cndmask_b32_e32 v16, v40, v16, vcc
	v_cndmask_b32_e32 v17, v40, v17, vcc
	v_cmp_gt_i32_e32 vcc, s4, v48
	v_pk_max_f16 v10, v10, v14
	v_pk_max_f16 v11, v11, v15
	v_or_b32_e32 v14, 0x140, v37
	ds_bpermute_b32 v15, v49, v3
	v_cndmask_b32_e32 v18, v40, v18, vcc
	v_cndmask_b32_e32 v19, v40, v19, vcc
	v_cndmask_b32_e32 v20, v40, v20, vcc
	v_cndmask_b32_e32 v21, v40, v21, vcc
	s_waitcnt lgkmcnt(1)
	v_pk_add_f16 v2, v2, v52
	v_cmp_gt_i32_e32 vcc, s4, v14
	v_pk_max_f16 v18, v18, v18
	s_waitcnt lgkmcnt(0)
	v_pk_add_f16 v3, v3, v15
	v_cndmask_b32_e32 v2, v40, v2, vcc
	v_pk_max_f16 v10, v10, v18
	v_pk_max_f16 v2, v2, v2
	v_pk_max_f16 v32, v32, v32
	v_pk_max_f16 v2, v10, v2
	ds_bpermute_b32 v10, v49, v4
	v_pk_max_f16 v19, v19, v19
	v_cndmask_b32_e32 v3, v40, v3, vcc
	v_pk_max_f16 v28, v28, v28
	v_pk_max_f16 v32, v32, s3 op_sel_hi:[1,0]
	v_pk_max_f16 v11, v11, v19
	v_pk_max_f16 v3, v3, v3
	v_pk_max_f16 v12, v12, v12
	v_pk_max_f16 v28, v32, v28
	v_pk_max_f16 v3, v11, v3
	ds_bpermute_b32 v11, v49, v5
	v_pk_max_f16 v16, v16, v16
	v_pk_max_f16 v12, v28, v12
	s_waitcnt lgkmcnt(1)
	v_pk_add_f16 v4, v4, v10
	s_waitcnt vmcnt(1)
	ds_bpermute_b32 v10, v49, v22
	v_pk_max_f16 v20, v20, v20
	v_pk_max_f16 v12, v12, v16
	v_cndmask_b32_e32 v4, v40, v4, vcc
	v_pk_max_f16 v12, v12, v20
	v_pk_max_f16 v4, v4, v4
	s_waitcnt lgkmcnt(1)
	v_pk_add_f16 v5, v5, v11
	v_pk_max_f16 v4, v12, v4
	ds_bpermute_b32 v12, v49, v23
	v_or_b32_e32 v11, 0x180, v37
	v_cndmask_b32_e32 v5, v40, v5, vcc
	s_waitcnt lgkmcnt(1)
	v_pk_add_f16 v10, v22, v10
	v_cmp_gt_i32_e32 vcc, s4, v11
	ds_bpermute_b32 v11, v49, v24
	v_pk_max_f16 v33, v33, v33
	v_cndmask_b32_e32 v10, v40, v10, vcc
	v_pk_max_f16 v10, v10, v10
	v_pk_max_f16 v29, v29, v29
	v_pk_max_f16 v2, v2, v10
	s_waitcnt lgkmcnt(1)
	v_pk_add_f16 v10, v23, v12
	s_waitcnt lgkmcnt(0)
	v_pk_add_f16 v11, v24, v11
	v_cndmask_b32_e32 v10, v40, v10, vcc
	v_pk_max_f16 v10, v10, v10
	v_cndmask_b32_e32 v11, v40, v11, vcc
	v_pk_max_f16 v3, v3, v10
	ds_bpermute_b32 v10, v49, v25
	v_pk_max_f16 v11, v11, v11
	v_pk_max_f16 v33, v33, s3 op_sel_hi:[1,0]
	v_pk_max_f16 v4, v4, v11
	s_waitcnt vmcnt(0)
	ds_bpermute_b32 v11, v49, v6
	v_pk_max_f16 v13, v13, v13
	v_pk_max_f16 v29, v33, v29
	v_pk_max_f16 v17, v17, v17
	v_pk_max_f16 v13, v29, v13
	v_pk_max_f16 v21, v21, v21
	v_pk_max_f16 v13, v13, v17
	s_waitcnt lgkmcnt(1)
	v_pk_add_f16 v10, v25, v10
	v_pk_max_f16 v13, v13, v21
	v_pk_max_f16 v5, v5, v5
	v_cndmask_b32_e32 v10, v40, v10, vcc
	v_pk_max_f16 v5, v13, v5
	v_pk_max_f16 v10, v10, v10
	s_waitcnt lgkmcnt(0)
	v_pk_add_f16 v6, v6, v11
	ds_bpermute_b32 v11, v49, v7
	v_pk_max_f16 v5, v5, v10
	v_or_b32_e32 v10, 0x1c0, v37
	v_cmp_gt_i32_e32 vcc, s4, v10
	s_nop 1
	v_cndmask_b32_e32 v6, v40, v6, vcc
	v_pk_max_f16 v6, v6, v6
	s_nop 0
	v_pk_max_f16 v2, v2, v6
	s_waitcnt lgkmcnt(0)
	v_pk_add_f16 v6, v7, v11
	ds_bpermute_b32 v7, v49, v8
	v_cndmask_b32_e32 v6, v40, v6, vcc
	v_pk_max_f16 v6, v6, v6
	s_waitcnt lgkmcnt(0)
	v_pk_add_f16 v7, v8, v7
	v_pk_max_f16 v6, v3, v6
	ds_bpermute_b32 v3, v49, v9
	v_cndmask_b32_e32 v7, v40, v7, vcc
	v_pk_max_f16 v7, v7, v7
	s_waitcnt lgkmcnt(0)
	v_pk_add_f16 v3, v9, v3
	s_nop 0
	v_cndmask_b32_e32 v3, v40, v3, vcc
	v_pk_max_f16 v7, v4, v7
	v_pk_max_f16 v3, v3, v3
	v_and_b32_e32 v4, 64, v1
	v_pk_max_f16 v9, v5, v3
	v_xor_b32_e32 v3, 16, v1
	v_add_u32_e32 v4, 64, v4
	v_cmp_lt_i32_e32 vcc, v3, v4
	s_nop 1
	v_cndmask_b32_e32 v3, v1, v3, vcc
	v_lshlrev_b32_e32 v8, 2, v3
	ds_bpermute_b32 v5, v8, v2
	v_xor_b32_e32 v3, 32, v1
	ds_bpermute_b32 v11, v8, v6
	v_cmp_lt_i32_e32 vcc, v3, v4
	s_nop 1
	v_cndmask_b32_e32 v3, v1, v3, vcc
	v_lshlrev_b32_e32 v10, 2, v3
	s_waitcnt lgkmcnt(1)
	v_pk_max_f16 v3, v5, v5
	s_waitcnt lgkmcnt(0)
	v_pk_max_f16 v5, v11, v11
	v_pk_max_f16 v3, v2, v3
	ds_bpermute_b32 v2, v8, v7
	ds_bpermute_b32 v11, v8, v9
	v_pk_max_f16 v5, v6, v5
	ds_bpermute_b32 v4, v10, v3
	ds_bpermute_b32 v6, v10, v5
	s_waitcnt lgkmcnt(3)
	v_pk_max_f16 v2, v2, v2
	v_cmp_gt_u32_e32 vcc, 8, v38
	v_pk_max_f16 v7, v7, v2
	s_waitcnt lgkmcnt(2)
	v_pk_max_f16 v2, v11, v11
	ds_bpermute_b32 v8, v10, v7
	v_pk_max_f16 v9, v9, v2
	ds_bpermute_b32 v10, v10, v9
	v_lshlrev_b32_e32 v2, 2, v0
	s_and_saveexec_b64 s[4:5], vcc
	s_cbranch_execz .LBB2_2
	s_waitcnt lgkmcnt(0)
	v_pk_max_f16 v10, v10, v10
	v_pk_max_f16 v9, v9, v9
	v_pk_max_f16 v8, v8, v8
	v_pk_max_f16 v7, v7, v7
	v_pk_max_f16 v6, v6, v6
	v_pk_max_f16 v5, v5, v5
	v_pk_max_f16 v4, v4, v4
	v_pk_max_f16 v3, v3, v3
	v_pk_max_f16 v11, v9, v10
	v_pk_max_f16 v9, v7, v8
	v_pk_max_f16 v7, v5, v6
	v_pk_max_f16 v3, v3, v4
	v_cvt_f32_f16_e32 v6, v7
	v_cvt_f32_f16_e32 v4, v3
	v_cvt_f32_f16_sdwa v5, v3 dst_sel:DWORD dst_unused:UNUSED_PAD src0_sel:WORD_1
	v_cvt_f32_f16_sdwa v7, v7 dst_sel:DWORD dst_unused:UNUSED_PAD src0_sel:WORD_1
	v_cvt_f32_f16_e32 v8, v9
	v_cvt_f32_f16_sdwa v9, v9 dst_sel:DWORD dst_unused:UNUSED_PAD src0_sel:WORD_1
	v_cvt_f32_f16_e32 v10, v11
	v_cvt_f32_f16_sdwa v11, v11 dst_sel:DWORD dst_unused:UNUSED_PAD src0_sel:WORD_1
	v_and_b32_e32 v3, 0xf00, v2
	v_lshl_add_u32 v3, v36, 5, v3
	ds_write_b128 v3, v[4:7]
	ds_write_b128 v3, v[8:11] offset:16

amdhsa.kernels:
  - .agpr_count:     0
    .args:
      - .actual_access:  read_only
        .address_space:  global
        .offset:         0
        .size:           8
        .value_kind:     global_buffer
      - .actual_access:  read_only
        .address_space:  global
        .offset:         8
        .size:           8
        .value_kind:     global_buffer
      - .actual_access:  write_only
        .address_space:  global
        .offset:         16
        .size:           8
        .value_kind:     global_buffer
      - .actual_access:  write_only
        .address_space:  global
        .offset:         24
        .size:           8
        .value_kind:     global_buffer
      - .actual_access:  write_only
        .address_space:  global
        .offset:         32
        .size:           8
        .value_kind:     global_buffer
      - .actual_access:  write_only
        .address_space:  global
        .offset:         40
        .size:           8
        .value_kind:     global_buffer
    .group_segment_fixed_size: 32
    .kernarg_segment_align: 8
    .kernarg_segment_size: 48
    .language:       OpenCL C
    .language_version:
      - 2
      - 0
    .max_flat_workgroup_size: 512
    .name:           _Z6k_prepPKiPKfPiS3_P15HIP_vector_typeIjLj4EEPh
    .private_segment_fixed_size: 0
    .sgpr_count:     16
    .sgpr_spill_count: 0
    .symbol:         _Z6k_prepPKiPKfPiS3_P15HIP_vector_typeIjLj4EEPh.kd
    .uniform_work_group_size: 1
    .uses_dynamic_stack: false
    .vgpr_count:     36
    .vgpr_spill_count: 0
    .wavefront_size: 64
  - .agpr_count:     0
    .args:
      - .actual_access:  read_only
        .address_space:  global
        .offset:         0
        .size:           8
        .value_kind:     global_buffer
      - .actual_access:  read_only
        .address_space:  global
        .offset:         8
        .size:           8
        .value_kind:     global_buffer
      - .actual_access:  read_only
        .address_space:  global
        .offset:         16
        .size:           8
        .value_kind:     global_buffer
      - .actual_access:  write_only
        .address_space:  global
        .offset:         24
        .size:           8
        .value_kind:     global_buffer
      - .actual_access:  read_only
        .address_space:  global
        .offset:         32
        .size:           8
        .value_kind:     global_buffer
    .group_segment_fixed_size: 0
    .kernarg_segment_align: 8
    .kernarg_segment_size: 40
    .language:       OpenCL C
    .language_version:
      - 2
      - 0
    .max_flat_workgroup_size: 256
    .name:           _Z6k_gemmPKfS0_PK15HIP_vector_typeIjLj4EEPDF16_PKh
    .private_segment_fixed_size: 0
    .sgpr_count:     48
    .sgpr_spill_count: 0
    .symbol:         _Z6k_gemmPKfS0_PK15HIP_vector_typeIjLj4EEPDF16_PKh.kd
    .uniform_work_group_size: 1
    .uses_dynamic_stack: false
    .vgpr_count:     230
    .vgpr_spill_count: 0
    .wavefront_size: 64
  - .agpr_count:     0
    .args:
      - .actual_access:  read_only
        .address_space:  global
        .offset:         0
        .size:           8
        .value_kind:     global_buffer
      - .actual_access:  read_only
        .address_space:  global
        .offset:         8
        .size:           8
        .value_kind:     global_buffer
      - .actual_access:  read_only
        .address_space:  global
        .offset:         16
        .size:           8
        .value_kind:     global_buffer
      - .actual_access:  read_only
        .address_space:  global
        .offset:         24
        .size:           8
        .value_kind:     global_buffer
      - .actual_access:  read_only
        .address_space:  global
        .offset:         32
        .size:           8
        .value_kind:     global_buffer
      - .actual_access:  read_only
        .address_space:  global
        .offset:         40
        .size:           8
        .value_kind:     global_buffer
      - .actual_access:  write_only
        .address_space:  global
        .offset:         48
        .size:           8
        .value_kind:     global_buffer
    .group_segment_fixed_size: 4096
    .kernarg_segment_align: 8
    .kernarg_segment_size: 56
    .language:       OpenCL C
    .language_version:
      - 2
      - 0
    .max_flat_workgroup_size: 1024
    .name:           _Z6k_poolPKDF16_PKiS2_PKfS4_S4_Pf
    .private_segment_fixed_size: 0
    .sgpr_count:     20
    .sgpr_spill_count: 0
    .symbol:         _Z6k_poolPKDF16_PKiS2_PKfS4_S4_Pf.kd
    .uniform_work_group_size: 1
    .uses_dynamic_stack: false
    .vgpr_count:     60
    .vgpr_spill_count: 0
    .wavefront_size: 64
